# speedup vs baseline: 1.0012x; 1.0012x over previous
.LBB2_15:
	ds_read_b64_tr_b16 v[178:179], v206 offset:40960
	ds_read_b64_tr_b16 v[180:181], v206 offset:41984
	s_waitcnt lgkmcnt(9)
	v_mfma_f32_32x32x16_f16 v[98:113], v[82:85], v[154:157], v[34:49]
	v_add_f32_e32 v224, v66, v70
	v_add_f32_e32 v225, v67, v71
	v_add_f32_e32 v226, v68, v72
	v_add_f32_e32 v227, v69, v73
	v_add_f32_e32 v224, v74, v224
	v_cvt_pk_f16_f32 v158, v66, v67
	v_cvt_pk_f16_f32 v159, v68, v69
	ds_read_b64_tr_b16 v[174:175], v207 offset:40960
	ds_read_b64_tr_b16 v[176:177], v207 offset:41984
	v_add_f32_e32 v225, v75, v225
	s_waitcnt lgkmcnt(10)
	v_mfma_f32_32x32x16_f16 v[82:97], v[170:173], v[154:157], v[34:49]
	v_add_f32_e32 v226, v76, v226
	v_add_f32_e32 v227, v77, v227
	v_add_f32_e32 v224, v78, v224
	v_cvt_pk_f16_f32 v160, v70, v71
	v_cvt_pk_f16_f32 v161, v72, v73
	ds_read_b64_tr_b16 v[170:171], v206 offset:43008
	ds_read_b64_tr_b16 v[172:173], v206 offset:44032
	s_waitcnt lgkmcnt(11)
	v_mfma_f32_32x32x16_f16 v[98:113], v[166:169], v[146:149], v[98:113]
	v_add_f32_e32 v225, v79, v225
	v_add_f32_e32 v226, v80, v226
	v_add_f32_e32 v227, v81, v227
	v_add_f32_e32 v224, v50, v224
	v_cvt_pk_f16_f32 v150, v74, v75
	v_cvt_pk_f16_f32 v151, v76, v77
	ds_read_b64_tr_b16 v[74:75], v207 offset:43008
	ds_read_b64_tr_b16 v[76:77], v207 offset:44032
	s_waitcnt lgkmcnt(12)
	v_mfma_f32_32x32x16_f16 v[82:97], v[162:165], v[146:149], v[82:97]
	v_add_f32_e32 v225, v51, v225
	v_add_f32_e32 v226, v52, v226
	v_add_f32_e32 v227, v53, v227
	v_add_f32_e32 v224, v54, v224
	v_cvt_pk_f16_f32 v152, v78, v79
	v_cvt_pk_f16_f32 v153, v80, v81
	ds_read_b64_tr_b16 v[70:71], v206 offset:45056
	ds_read_b64_tr_b16 v[72:73], v206 offset:46080
	s_waitcnt lgkmcnt(13)
	v_mfma_f32_32x32x16_f16 v[98:113], v[126:129], v[138:141], v[98:113]
	v_add_f32_e32 v225, v55, v225
	v_add_f32_e32 v226, v56, v226
	v_add_f32_e32 v227, v57, v227
	v_add_f32_e32 v224, v58, v224
	v_cvt_pk_f16_f32 v142, v50, v51
	v_cvt_pk_f16_f32 v143, v52, v53
	ds_read_b64_tr_b16 v[66:67], v207 offset:45056
	ds_read_b64_tr_b16 v[68:69], v207 offset:46080
	s_waitcnt lgkmcnt(14)
	v_mfma_f32_32x32x16_f16 v[82:97], v[122:125], v[138:141], v[82:97]
	v_add_f32_e32 v225, v59, v225
	v_add_f32_e32 v226, v60, v226
	v_add_f32_e32 v227, v61, v227
	v_add_f32_e32 v224, v62, v224
	v_cvt_pk_f16_f32 v144, v54, v55
	v_cvt_pk_f16_f32 v145, v56, v57
	ds_read_b64_tr_b16 v[54:55], v206 offset:47104
	ds_read_b64_tr_b16 v[56:57], v206 offset:48128
	s_waitcnt lgkmcnt(14)
	v_mfma_f32_32x32x16_f16 v[98:113], v[118:121], v[134:137], v[98:113]
	v_add_f32_e32 v225, v63, v225
	v_add_f32_e32 v226, v64, v226
	v_add_f32_e32 v227, v65, v227
	v_add_f32_e32 v224, v224, v225
	v_cvt_pk_f16_f32 v130, v58, v59
	v_cvt_pk_f16_f32 v131, v60, v61
	ds_read_b64_tr_b16 v[50:51], v207 offset:47104
	ds_read_b64_tr_b16 v[52:53], v207 offset:48128
	v_mfma_f32_32x32x16_f16 v[82:97], v[114:117], v[134:137], v[82:97]
	v_add_f32_e32 v226, v226, v227
	v_add_f32_e32 v58, v224, v226
	v_add_f32_e32 v58, 0, v58
	v_cvt_pk_f16_f32 v132, v62, v63
	v_cvt_pk_f16_f32 v133, v64, v65
	s_mov_b64 s[2:3], 0x3c000
	v_add_f32_e32 v214, v183, v58
	v_lshl_add_u64 v[58:59], v[186:187], 0, s[2:3]
	s_mov_b32 s2, m0
	s_mov_b32 m0, s36
	s_nop 0
	global_load_lds_dwordx4 v[58:59], off
	s_mov_b32 m0, s2
	s_mov_b64 s[2:3], 0x38000
	v_lshl_add_u64 v[58:59], v[194:195], 0, s[2:3]
	s_mov_b32 s2, m0
	s_mov_b32 m0, s34
	s_nop 0
	global_load_lds_dwordx4 v[58:59], off
	s_mov_b32 m0, s2
	v_max_f32_e32 v58, v99, v99
	v_max_f32_e32 v59, v98, v98
	v_max_f32_e32 v58, v59, v58
	v_max3_f32 v59, v100, v101, v83
	v_max3_f32 v58, v58, v82, v84
	v_max3_f32 v58, v58, v85, v102
	v_max3_f32 v59, v59, v104, v105
	v_max3_f32 v58, v58, v103, v86
	v_max3_f32 v59, v59, v88, v89
	v_max3_f32 v58, v58, v87, v106
	v_max3_f32 v59, v59, v108, v109
	v_max3_f32 v58, v58, v107, v90
	v_max3_f32 v59, v59, v92, v93
	v_max3_f32 v58, v58, v91, v110
	v_max3_f32 v59, v59, v112, v113
	v_max3_f32 v58, v58, v111, v94
	v_max3_f32 v59, v59, v96, v97
	v_max3_f32 v58, v58, v95, v59
	v_mov_b32_e32 v59, v58
	s_nop 1
	v_permlane32_swap_b32_e32 v58, v59
	v_max_f32_e32 v59, v59, v59
	v_max_f32_e32 v58, v58, v58
	v_max_f32_e32 v58, v58, v59
	s_mov_b32 s2, 0x41000000
	v_cmp_lt_f32_e32 vcc, s2, v58
	s_cmp_lg_u64 vcc, 0
	s_mov_b64 s[20:21], 0x36000
	s_cselect_b64 s[2:3], -1, 0
	s_cbranch_vccnz .LBB2_65

.LBB2_18:
	ds_read_b64_tr_b16 v[166:167], v206 offset:24576
	ds_read_b64_tr_b16 v[168:169], v206 offset:25600
	s_waitcnt lgkmcnt(9)
	v_mfma_f32_32x32x16_f16 v[114:129], v[58:61], v[154:157], v[34:49]
	v_add_f32_e32 v224, v98, v102
	v_add_f32_e32 v225, v99, v103
	v_add_f32_e32 v226, v100, v104
	v_add_f32_e32 v227, v101, v105
	v_add_f32_e32 v224, v106, v224
	v_cvt_pk_f16_f32 v158, v98, v99
	v_cvt_pk_f16_f32 v159, v100, v101
	ds_read_b64_tr_b16 v[162:163], v207 offset:24576
	ds_read_b64_tr_b16 v[164:165], v207 offset:25600
	v_add_f32_e32 v225, v107, v225
	v_add_f32_e32 v226, v108, v226
	v_add_f32_e32 v227, v109, v227
	v_add_f32_e32 v224, v110, v224
	s_waitcnt lgkmcnt(10)
	v_mfma_f32_32x32x16_f16 v[50:65], v[182:185], v[154:157], v[34:49]
	v_cvt_pk_f16_f32 v160, v102, v103
	v_cvt_pk_f16_f32 v161, v104, v105
	ds_read_b64_tr_b16 v[102:103], v206 offset:26624
	ds_read_b64_tr_b16 v[104:105], v206 offset:27648
	s_waitcnt lgkmcnt(11)
	v_mfma_f32_32x32x16_f16 v[114:129], v[186:189], v[146:149], v[114:129]
	v_add_f32_e32 v225, v111, v225
	v_add_f32_e32 v226, v112, v226
	v_add_f32_e32 v227, v113, v227
	v_add_f32_e32 v224, v82, v224
	v_cvt_pk_f16_f32 v150, v106, v107
	v_cvt_pk_f16_f32 v151, v108, v109
	ds_read_b64_tr_b16 v[98:99], v207 offset:26624
	ds_read_b64_tr_b16 v[100:101], v207 offset:27648
	s_waitcnt lgkmcnt(12)
	v_mfma_f32_32x32x16_f16 v[50:65], v[78:81], v[146:149], v[50:65]
	v_add_f32_e32 v225, v83, v225
	v_add_f32_e32 v226, v84, v226
	v_add_f32_e32 v227, v85, v227
	v_add_f32_e32 v224, v86, v224
	v_cvt_pk_f16_f32 v152, v110, v111
	v_cvt_pk_f16_f32 v153, v112, v113
	ds_read_b64_tr_b16 v[78:79], v206 offset:28672
	ds_read_b64_tr_b16 v[80:81], v206 offset:29696
	s_waitcnt lgkmcnt(13)
	v_mfma_f32_32x32x16_f16 v[114:129], v[74:77], v[138:141], v[114:129]
	v_add_f32_e32 v225, v87, v225
	v_add_f32_e32 v226, v88, v226
	v_add_f32_e32 v227, v89, v227
	v_add_f32_e32 v224, v90, v224
	v_cvt_pk_f16_f32 v142, v82, v83
	v_cvt_pk_f16_f32 v143, v84, v85
	ds_read_b64_tr_b16 v[74:75], v207 offset:28672
	ds_read_b64_tr_b16 v[76:77], v207 offset:29696
	s_waitcnt lgkmcnt(14)
	v_mfma_f32_32x32x16_f16 v[50:65], v[174:177], v[138:141], v[50:65]
	v_add_f32_e32 v225, v91, v225
	v_add_f32_e32 v226, v92, v226
	v_add_f32_e32 v227, v93, v227
	v_add_f32_e32 v224, v94, v224
	v_cvt_pk_f16_f32 v144, v86, v87
	v_cvt_pk_f16_f32 v145, v88, v89
	ds_read_b64_tr_b16 v[70:71], v206 offset:30720
	ds_read_b64_tr_b16 v[72:73], v206 offset:31744
	s_waitcnt lgkmcnt(14)
	v_mfma_f32_32x32x16_f16 v[114:129], v[178:181], v[134:137], v[114:129]
	v_add_f32_e32 v225, v95, v225
	v_add_f32_e32 v226, v96, v226
	v_add_f32_e32 v227, v97, v227
	v_add_f32_e32 v224, v224, v225
	v_cvt_pk_f16_f32 v130, v90, v91
	v_cvt_pk_f16_f32 v131, v92, v93
	ds_read_b64_tr_b16 v[66:67], v207 offset:30720
	ds_read_b64_tr_b16 v[68:69], v207 offset:31744
	v_mfma_f32_32x32x16_f16 v[50:65], v[170:173], v[134:137], v[50:65]
	v_add_f32_e32 v226, v226, v227
	v_add_f32_e32 v82, v224, v226
	v_add_f32_e32 v82, 0, v82
	v_cvt_pk_f16_f32 v132, v94, v95
	v_cvt_pk_f16_f32 v133, v96, v97
	s_mov_b64 s[2:3], 0x8000
	v_add_f32_e32 v182, v214, v82
	v_lshl_add_u64 v[82:83], v[198:199], 0, s[2:3]
	s_mov_b32 s2, m0
	s_mov_b32 m0, s37
	s_nop 0
	global_load_lds_dwordx4 v[82:83], off
	s_mov_b32 m0, s2
	s_mov_b64 s[2:3], 0x4000
	v_lshl_add_u64 v[82:83], v[196:197], 0, s[2:3]
	s_add_i32 s2, s36, 0xa000
	s_mov_b32 s3, m0
	s_mov_b32 m0, s2
	s_nop 0
	global_load_lds_dwordx4 v[82:83], off
	s_mov_b32 m0, s3
	v_max_f32_e32 v82, v115, v115
	v_max_f32_e32 v83, v114, v114
	v_max_f32_e32 v82, v83, v82
	v_max3_f32 v83, v116, v117, v51
	v_max3_f32 v82, v82, v50, v52
	v_max3_f32 v82, v82, v53, v118
	v_max3_f32 v83, v83, v120, v121
	v_max3_f32 v82, v82, v119, v54
	v_max3_f32 v83, v83, v56, v57
	v_max3_f32 v82, v82, v55, v122
	v_max3_f32 v83, v83, v124, v125
	v_max3_f32 v82, v82, v123, v58
	v_max3_f32 v83, v83, v60, v61
	v_max3_f32 v82, v82, v59, v126
	v_max3_f32 v83, v83, v128, v129
	v_max3_f32 v82, v82, v127, v62
	v_max3_f32 v83, v83, v64, v65
	v_max3_f32 v82, v82, v63, v83
	v_mov_b32_e32 v83, v82
	s_nop 1
	v_permlane32_swap_b32_e32 v82, v83
	v_max_f32_e32 v83, v83, v83
	v_max_f32_e32 v82, v82, v82
	v_max_f32_e32 v82, v82, v83
	s_mov_b32 s2, 0x41000000
	v_cmp_lt_f32_e32 vcc, s2, v82
	s_cmp_lg_u64 vcc, 0
	s_cselect_b64 s[2:3], -1, 0
	s_cbranch_vccnz .LBB2_68

.LBB2_21:
	ds_read_b64_tr_b16 v[162:163], v206 offset:32768
	ds_read_b64_tr_b16 v[164:165], v206 offset:33792
	s_waitcnt lgkmcnt(9)
	v_mfma_f32_32x32x16_f16 v[82:97], v[110:113], v[154:157], v[34:49]
	v_add_f32_e32 v224, v114, v118
	v_add_f32_e32 v225, v115, v119
	v_add_f32_e32 v226, v116, v120
	v_add_f32_e32 v227, v117, v121
	v_add_f32_e32 v224, v122, v224
	v_cvt_pk_f16_f32 v158, v114, v115
	v_cvt_pk_f16_f32 v159, v116, v117
	ds_read_b64_tr_b16 v[114:115], v207 offset:32768
	ds_read_b64_tr_b16 v[116:117], v207 offset:33792
	v_add_f32_e32 v225, v123, v225
	v_add_f32_e32 v226, v124, v226
	v_add_f32_e32 v227, v125, v227
	v_add_f32_e32 v224, v126, v224
	s_waitcnt lgkmcnt(10)
	v_mfma_f32_32x32x16_f16 v[66:81], v[106:109], v[154:157], v[34:49]
	v_cvt_pk_f16_f32 v160, v118, v119
	v_cvt_pk_f16_f32 v161, v120, v121
	ds_read_b64_tr_b16 v[110:111], v206 offset:34816
	ds_read_b64_tr_b16 v[112:113], v206 offset:35840
	s_waitcnt lgkmcnt(11)
	v_mfma_f32_32x32x16_f16 v[82:97], v[178:181], v[146:149], v[82:97]
	v_add_f32_e32 v225, v127, v225
	v_add_f32_e32 v226, v128, v226
	v_add_f32_e32 v227, v129, v227
	v_add_f32_e32 v224, v50, v224
	v_cvt_pk_f16_f32 v150, v122, v123
	v_cvt_pk_f16_f32 v151, v124, v125
	ds_read_b64_tr_b16 v[106:107], v207 offset:34816
	ds_read_b64_tr_b16 v[108:109], v207 offset:35840
	s_waitcnt lgkmcnt(12)
	v_mfma_f32_32x32x16_f16 v[66:81], v[102:105], v[146:149], v[66:81]
	v_add_f32_e32 v225, v51, v225
	v_add_f32_e32 v226, v52, v226
	v_add_f32_e32 v227, v53, v227
	v_add_f32_e32 v224, v54, v224
	v_cvt_pk_f16_f32 v152, v126, v127
	v_cvt_pk_f16_f32 v153, v128, v129
	ds_read_b64_tr_b16 v[102:103], v206 offset:36864
	ds_read_b64_tr_b16 v[104:105], v206 offset:37888
	s_waitcnt lgkmcnt(13)
	v_mfma_f32_32x32x16_f16 v[82:97], v[98:101], v[138:141], v[82:97]
	v_add_f32_e32 v225, v55, v225
	v_add_f32_e32 v226, v56, v226
	v_add_f32_e32 v227, v57, v227
	v_add_f32_e32 v224, v58, v224
	v_cvt_pk_f16_f32 v142, v50, v51
	v_cvt_pk_f16_f32 v143, v52, v53
	ds_read_b64_tr_b16 v[98:99], v207 offset:36864
	ds_read_b64_tr_b16 v[100:101], v207 offset:37888
	s_waitcnt lgkmcnt(14)
	v_mfma_f32_32x32x16_f16 v[66:81], v[170:173], v[138:141], v[66:81]
	v_add_f32_e32 v225, v59, v225
	v_add_f32_e32 v226, v60, v226
	v_add_f32_e32 v227, v61, v227
	v_add_f32_e32 v224, v62, v224
	v_cvt_pk_f16_f32 v144, v54, v55
	v_cvt_pk_f16_f32 v145, v56, v57
	ds_read_b64_tr_b16 v[54:55], v206 offset:38912
	ds_read_b64_tr_b16 v[56:57], v206 offset:39936
	s_waitcnt lgkmcnt(14)
	v_mfma_f32_32x32x16_f16 v[82:97], v[174:177], v[134:137], v[82:97]
	v_add_f32_e32 v225, v63, v225
	v_add_f32_e32 v226, v64, v226
	v_add_f32_e32 v227, v65, v227
	v_add_f32_e32 v224, v224, v225
	v_cvt_pk_f16_f32 v130, v58, v59
	v_cvt_pk_f16_f32 v131, v60, v61
	ds_read_b64_tr_b16 v[50:51], v207 offset:38912
	ds_read_b64_tr_b16 v[52:53], v207 offset:39936
	v_mfma_f32_32x32x16_f16 v[66:81], v[166:169], v[134:137], v[66:81]
	v_add_f32_e32 v226, v226, v227
	v_add_f32_e32 v58, v224, v226
	v_add_f32_e32 v58, 0, v58
	v_cvt_pk_f16_f32 v132, v62, v63
	v_cvt_pk_f16_f32 v133, v64, v65
	s_mov_b64 s[2:3], 0x3c000
	v_add_f32_e32 v184, v182, v58
	v_lshl_add_u64 v[58:59], v[194:195], 0, s[2:3]
	s_mov_b32 s2, m0
	s_mov_b32 m0, s35
	s_nop 0
	global_load_lds_dwordx4 v[58:59], off
	s_mov_b32 m0, s2
	v_max_f32_e32 v58, v83, v83
	v_max_f32_e32 v59, v82, v82
	v_max_f32_e32 v58, v59, v58
	s_nop 0
	v_max3_f32 v59, v84, v85, v67
	v_max3_f32 v58, v58, v66, v68
	v_max3_f32 v58, v58, v69, v86
	v_max3_f32 v59, v59, v88, v89
	v_max3_f32 v58, v58, v87, v70
	v_max3_f32 v59, v59, v72, v73
	v_max3_f32 v58, v58, v71, v90
	v_max3_f32 v59, v59, v92, v93
	v_max3_f32 v58, v58, v91, v74
	v_max3_f32 v59, v59, v76, v77
	v_max3_f32 v58, v58, v75, v94
	v_max3_f32 v59, v59, v96, v97
	v_max3_f32 v58, v58, v95, v78
	v_max3_f32 v59, v59, v80, v81
	v_max3_f32 v58, v58, v79, v59
	v_mov_b32_e32 v59, v58
	s_nop 1
	v_permlane32_swap_b32_e32 v58, v59
	v_max_f32_e32 v59, v59, v59
	v_max_f32_e32 v58, v58, v58
	v_max_f32_e32 v58, v58, v59
	s_mov_b32 s2, 0x41000000
	v_cmp_lt_f32_e32 vcc, s2, v58
	s_cmp_lg_u64 vcc, 0
	s_mov_b64 s[20:21], 0x3a000
	s_cselect_b64 s[2:3], -1, 0
	s_cbranch_vccnz .LBB2_71

.LBB2_24:
	ds_read_b64_tr_b16 v[122:123], v206 offset:40960
	ds_read_b64_tr_b16 v[124:125], v206 offset:41984
	s_waitcnt lgkmcnt(9)
	v_mfma_f32_32x32x16_f16 v[98:113], v[58:61], v[154:157], v[34:49]
	v_add_f32_e32 v224, v82, v86
	v_add_f32_e32 v225, v83, v87
	v_add_f32_e32 v226, v84, v88
	v_add_f32_e32 v227, v85, v89
	v_add_f32_e32 v224, v90, v224
	v_cvt_pk_f16_f32 v158, v82, v83
	v_cvt_pk_f16_f32 v159, v84, v85
	ds_read_b64_tr_b16 v[118:119], v207 offset:40960
	ds_read_b64_tr_b16 v[120:121], v207 offset:41984
	v_add_f32_e32 v225, v91, v225
	v_add_f32_e32 v226, v92, v226
	v_add_f32_e32 v227, v93, v227
	v_add_f32_e32 v224, v94, v224
	s_waitcnt lgkmcnt(10)
	v_mfma_f32_32x32x16_f16 v[50:65], v[114:117], v[154:157], v[34:49]
	v_cvt_pk_f16_f32 v160, v86, v87
	v_cvt_pk_f16_f32 v161, v88, v89
	ds_read_b64_tr_b16 v[114:115], v206 offset:43008
	ds_read_b64_tr_b16 v[116:117], v206 offset:44032
	s_waitcnt lgkmcnt(11)
	v_mfma_f32_32x32x16_f16 v[98:113], v[178:181], v[146:149], v[98:113]
	v_add_f32_e32 v225, v95, v225
	v_add_f32_e32 v226, v96, v226
	v_add_f32_e32 v227, v97, v227
	v_add_f32_e32 v224, v66, v224
	v_cvt_pk_f16_f32 v150, v90, v91
	v_cvt_pk_f16_f32 v151, v92, v93
	ds_read_b64_tr_b16 v[90:91], v207 offset:43008
	ds_read_b64_tr_b16 v[92:93], v207 offset:44032
	s_waitcnt lgkmcnt(12)
	v_mfma_f32_32x32x16_f16 v[50:65], v[170:173], v[146:149], v[50:65]
	v_add_f32_e32 v225, v67, v225
	v_add_f32_e32 v226, v68, v226
	v_add_f32_e32 v227, v69, v227
	v_add_f32_e32 v224, v70, v224
	v_cvt_pk_f16_f32 v152, v94, v95
	v_cvt_pk_f16_f32 v153, v96, v97
	ds_read_b64_tr_b16 v[86:87], v206 offset:45056
	ds_read_b64_tr_b16 v[88:89], v206 offset:46080
	s_waitcnt lgkmcnt(13)
	v_mfma_f32_32x32x16_f16 v[98:113], v[174:177], v[138:141], v[98:113]
	v_add_f32_e32 v225, v71, v225
	v_add_f32_e32 v226, v72, v226
	v_add_f32_e32 v227, v73, v227
	v_add_f32_e32 v224, v74, v224
	v_cvt_pk_f16_f32 v142, v66, v67
	v_cvt_pk_f16_f32 v143, v68, v69
	ds_read_b64_tr_b16 v[82:83], v207 offset:45056
	ds_read_b64_tr_b16 v[84:85], v207 offset:46080
	s_waitcnt lgkmcnt(14)
	v_mfma_f32_32x32x16_f16 v[50:65], v[162:165], v[138:141], v[50:65]
	v_add_f32_e32 v225, v75, v225
	v_add_f32_e32 v226, v76, v226
	v_add_f32_e32 v227, v77, v227
	v_add_f32_e32 v224, v78, v224
	v_cvt_pk_f16_f32 v144, v70, v71
	v_cvt_pk_f16_f32 v145, v72, v73
	ds_read_b64_tr_b16 v[70:71], v206 offset:47104
	ds_read_b64_tr_b16 v[72:73], v206 offset:48128
	s_waitcnt lgkmcnt(14)
	v_mfma_f32_32x32x16_f16 v[98:113], v[166:169], v[134:137], v[98:113]
	v_add_f32_e32 v225, v79, v225
	v_add_f32_e32 v226, v80, v226
	v_add_f32_e32 v227, v81, v227
	v_add_f32_e32 v224, v224, v225
	v_cvt_pk_f16_f32 v130, v74, v75
	v_cvt_pk_f16_f32 v131, v76, v77
	ds_read_b64_tr_b16 v[66:67], v207 offset:47104
	ds_read_b64_tr_b16 v[68:69], v207 offset:48128
	v_mfma_f32_32x32x16_f16 v[50:65], v[126:129], v[134:137], v[50:65]
	v_add_f32_e32 v226, v226, v227
	v_add_f32_e32 v74, v224, v226
	v_add_f32_e32 v74, 0, v74
	v_cvt_pk_f16_f32 v132, v78, v79
	v_cvt_pk_f16_f32 v133, v80, v81
	s_mov_b64 s[2:3], 0x4000
	v_add_f32_e32 v174, v184, v74
	v_lshl_add_u64 v[74:75], v[182:183], 0, s[2:3]
	s_mov_b32 s2, m0
	s_mov_b32 m0, s34
	s_nop 0
	global_load_lds_dwordx4 v[74:75], off
	s_mov_b32 m0, s2
	v_max_f32_e32 v74, v99, v99
	v_max_f32_e32 v75, v98, v98
	v_max_f32_e32 v74, v75, v74
	s_nop 0
	v_max3_f32 v75, v100, v101, v51
	v_max3_f32 v74, v74, v50, v52
	v_max3_f32 v74, v74, v53, v102
	v_max3_f32 v75, v75, v104, v105
	v_max3_f32 v74, v74, v103, v54
	v_max3_f32 v75, v75, v56, v57
	v_max3_f32 v74, v74, v55, v106
	v_max3_f32 v75, v75, v108, v109
	v_max3_f32 v74, v74, v107, v58
	v_max3_f32 v75, v75, v60, v61
	v_max3_f32 v74, v74, v59, v110
	v_max3_f32 v75, v75, v112, v113
	v_max3_f32 v74, v74, v111, v62
	v_max3_f32 v75, v75, v64, v65
	v_max3_f32 v74, v74, v63, v75
	v_mov_b32_e32 v75, v74
	s_nop 1
	v_permlane32_swap_b32_e32 v74, v75
	v_max_f32_e32 v75, v75, v75
	v_max_f32_e32 v74, v74, v74
	v_max_f32_e32 v74, v74, v75
	s_mov_b32 s2, 0x41000000
	v_cmp_lt_f32_e32 vcc, s2, v74
	s_cmp_lg_u64 vcc, 0
	s_cselect_b64 s[2:3], -1, 0
	s_cbranch_vccnz .LBB2_74

.LBB2_27:
	ds_read_b64_tr_b16 v[122:123], v206 offset:24576
	ds_read_b64_tr_b16 v[124:125], v206 offset:25600
	v_add_f32_e32 v224, v98, v102
	v_add_f32_e32 v225, v99, v103
	v_add_f32_e32 v226, v100, v104
	v_add_f32_e32 v227, v101, v105
	v_add_f32_e32 v224, v106, v224
	s_waitcnt lgkmcnt(9)
	v_mfma_f32_32x32x16_f16 v[66:81], v[118:121], v[154:157], v[34:49]
	v_cvt_pk_f16_f32 v158, v98, v99
	v_cvt_pk_f16_f32 v159, v100, v101
	ds_read_b64_tr_b16 v[118:119], v207 offset:24576
	ds_read_b64_tr_b16 v[120:121], v207 offset:25600
	s_waitcnt lgkmcnt(10)
	v_mfma_f32_32x32x16_f16 v[34:49], v[166:169], v[154:157], v[34:49]
	v_add_f32_e32 v225, v107, v225
	v_add_f32_e32 v226, v108, v226
	v_add_f32_e32 v227, v109, v227
	v_add_f32_e32 v224, v110, v224
	v_cvt_pk_f16_f32 v160, v102, v103
	v_cvt_pk_f16_f32 v161, v104, v105
	ds_read_b64_tr_b16 v[114:115], v206 offset:26624
	ds_read_b64_tr_b16 v[116:117], v206 offset:27648
	s_waitcnt lgkmcnt(11)
	v_mfma_f32_32x32x16_f16 v[66:81], v[170:173], v[146:149], v[66:81]
	v_add_f32_e32 v225, v111, v225
	v_add_f32_e32 v226, v112, v226
	v_add_f32_e32 v227, v113, v227
	v_add_f32_e32 v224, v50, v224
	v_cvt_pk_f16_f32 v150, v106, v107
	v_cvt_pk_f16_f32 v151, v108, v109
	ds_read_b64_tr_b16 v[102:103], v207 offset:26624
	ds_read_b64_tr_b16 v[104:105], v207 offset:27648
	s_waitcnt lgkmcnt(12)
	v_mfma_f32_32x32x16_f16 v[34:49], v[94:97], v[146:149], v[34:49]
	v_add_f32_e32 v225, v51, v225
	v_add_f32_e32 v226, v52, v226
	v_add_f32_e32 v227, v53, v227
	v_add_f32_e32 v224, v54, v224
	v_cvt_pk_f16_f32 v152, v110, v111
	v_cvt_pk_f16_f32 v153, v112, v113
	ds_read_b64_tr_b16 v[98:99], v206 offset:28672
	ds_read_b64_tr_b16 v[100:101], v206 offset:29696
	s_waitcnt lgkmcnt(13)
	v_mfma_f32_32x32x16_f16 v[66:81], v[162:165], v[138:141], v[66:81]
	v_add_f32_e32 v225, v55, v225
	v_add_f32_e32 v226, v56, v226
	v_add_f32_e32 v227, v57, v227
	v_add_f32_e32 v224, v58, v224
	v_cvt_pk_f16_f32 v142, v50, v51
	v_cvt_pk_f16_f32 v143, v52, v53
	ds_read_b64_tr_b16 v[94:95], v207 offset:28672
	ds_read_b64_tr_b16 v[96:97], v207 offset:29696
	s_waitcnt lgkmcnt(14)
	v_mfma_f32_32x32x16_f16 v[34:49], v[90:93], v[138:141], v[34:49]
	v_add_f32_e32 v225, v59, v225
	v_add_f32_e32 v226, v60, v226
	v_add_f32_e32 v227, v61, v227
	v_add_f32_e32 v224, v62, v224
	v_cvt_pk_f16_f32 v144, v54, v55
	v_cvt_pk_f16_f32 v145, v56, v57
	ds_read_b64_tr_b16 v[90:91], v206 offset:30720
	ds_read_b64_tr_b16 v[92:93], v206 offset:31744
	s_waitcnt lgkmcnt(14)
	v_mfma_f32_32x32x16_f16 v[66:81], v[126:129], v[134:137], v[66:81]
	v_add_f32_e32 v225, v63, v225
	v_add_f32_e32 v226, v64, v226
	v_add_f32_e32 v227, v65, v227
	v_add_f32_e32 v224, v224, v225
	v_cvt_pk_f16_f32 v130, v58, v59
	v_cvt_pk_f16_f32 v131, v60, v61
	ds_read_b64_tr_b16 v[82:83], v207 offset:30720
	ds_read_b64_tr_b16 v[84:85], v207 offset:31744
	v_mfma_f32_32x32x16_f16 v[34:49], v[86:89], v[134:137], v[34:49]
	v_add_f32_e32 v226, v226, v227
	v_add_f32_e32 v50, v224, v226
	v_add_f32_e32 v50, 0, v50
	v_cvt_pk_f16_f32 v132, v62, v63
	v_cvt_pk_f16_f32 v133, v64, v65
	s_cmp_lg_u32 s91, 0
	s_cbranch_scc1 .Lattn_pf_skip
	s_waitcnt lgkmcnt(0)
	s_barrier
	v_bfe_u32 v221, v0, 3, 3
	v_lshl_or_b32 v221, s33, 3, v221
	v_lshrrev_b32_e32 v222, 1, v221
	v_xor_b32_e32 v222, v222, v0
	v_lshlrev_b32_e32 v222, 4, v222
	v_and_b32_e32 v222, 0x70, v222
	v_lshl_or_b32 v221, v221, 7, v222
	s_mov_b32 m0, s36
	s_nop 0
	global_load_lds_dwordx4 v221, s[14:15]
	s_mov_b32 m0, s35
	s_nop 0
	global_load_lds_dwordx4 v[194:195], off
	s_add_u32 s44, s14, 0x2000
	s_addc_u32 s45, s15, 0
	s_add_i32 s46, s36, 0x2000
	s_mov_b32 m0, s46
	s_nop 0
	global_load_lds_dwordx4 v221, s[44:45]
	s_xor_b32 s48, s12, 0x700
	s_lshl_b32 s49, s18, 15
	s_or_b32 s48, s48, s49
	s_lshl_b32 s49, s30, 11
	s_or_b32 s48, s48, s49
	s_add_u32 s48, s48, s31
	s_mov_b32 s49, 0
	s_lshl_b64 s[48:49], s[48:49], 7
	s_add_u32 s48, s4, s48
	s_addc_u32 s49, s5, s49
	v_lshlrev_b32_e32 v223, 1, v192
	global_load_dwordx4 v[154:157], v223, s[48:49]
	global_load_dwordx4 v[146:149], v223, s[48:49] offset:32
	global_load_dwordx4 v[138:141], v223, s[48:49] offset:64
	global_load_dwordx4 v[134:137], v223, s[48:49] offset:96
	s_add_u32 s44, s14, 0x4000
	s_addc_u32 s45, s15, 0
	s_add_i32 s46, s36, 0x4000
	s_mov_b32 m0, s46
	s_nop 0
	global_load_lds_dwordx4 v221, s[44:45]

.LBB2_30:
	v_add_f32_e32 v224, v66, v70
	v_add_f32_e32 v225, v67, v71
	v_add_f32_e32 v226, v68, v72
	v_add_f32_e32 v227, v69, v73
	v_add_f32_e32 v224, v74, v224
	v_add_f32_e32 v225, v75, v225
	v_add_f32_e32 v226, v76, v226
	v_add_f32_e32 v227, v77, v227
	v_add_f32_e32 v224, v78, v224
	v_add_f32_e32 v225, v79, v225
	v_add_f32_e32 v226, v80, v226
	v_add_f32_e32 v227, v81, v227
	v_add_f32_e32 v224, v34, v224
	v_add_f32_e32 v225, v35, v225
	v_add_f32_e32 v226, v36, v226
	v_add_f32_e32 v227, v37, v227
	v_add_f32_e32 v224, v38, v224
	v_add_f32_e32 v225, v39, v225
	v_add_f32_e32 v226, v40, v226
	v_add_f32_e32 v227, v41, v227
	v_add_f32_e32 v224, v42, v224
	v_add_f32_e32 v225, v43, v225
	v_add_f32_e32 v226, v44, v226
	v_add_f32_e32 v227, v45, v227
	v_add_f32_e32 v224, v46, v224
	v_add_f32_e32 v225, v47, v225
	v_add_f32_e32 v226, v48, v226
	v_add_f32_e32 v227, v49, v227
	v_add_f32_e32 v224, v224, v225
	v_add_f32_e32 v226, v226, v227
	v_add_f32_e32 v50, v224, v226
	v_add_f32_e32 v50, v86, v50
	v_cvt_pk_f16_f32 v34, v34, v35
	v_cvt_pk_f16_f32 v52, v66, v67
	v_cvt_pk_f16_f32 v53, v68, v69
	v_cvt_pk_f16_f32 v54, v70, v71
	v_cvt_pk_f16_f32 v55, v72, v73
	v_cvt_pk_f16_f32 v56, v74, v75
	v_cvt_pk_f16_f32 v57, v76, v77
	v_cvt_pk_f16_f32 v58, v78, v79
	v_cvt_pk_f16_f32 v59, v80, v81
	v_cvt_pk_f16_f32 v35, v36, v37
	v_cvt_pk_f16_f32 v36, v38, v39
	v_cvt_pk_f16_f32 v37, v40, v41
	v_cvt_pk_f16_f32 v38, v42, v43
	v_cvt_pk_f16_f32 v39, v44, v45
	v_cvt_pk_f16_f32 v40, v46, v47
	v_cvt_pk_f16_f32 v41, v48, v49
	v_or_b32_e32 v42, 0x8000, v203
	v_add_u32_e32 v199, v42, v200
	v_add_u32_e32 v197, v42, v202
	ds_read_b64_tr_b16 v[42:43],v199 offset:0
	ds_read_b64_tr_b16 v[44:45],v199 offset:1024
	ds_read_b64_tr_b16 v[46:47],v199 offset:2048
	ds_read_b64_tr_b16 v[48:49],v199 offset:3072
	ds_read_b64_tr_b16 v[60:61],v199 offset:4096
	ds_read_b64_tr_b16 v[62:63],v199 offset:5120
	ds_read_b64_tr_b16 v[64:65],v199 offset:6144
	ds_read_b64_tr_b16 v[66:67],v199 offset:7168
	s_waitcnt lgkmcnt(0)
	s_nop 0
	v_mfma_f32_32x32x16_f16 v[2:17], v[52:55], v[42:45], v[2:17]
	ds_read_b64_tr_b16 v[42:43],v197 offset:0
	ds_read_b64_tr_b16 v[44:45],v197 offset:1024
	v_mfma_f32_32x32x16_f16 v[2:17], v[56:59], v[46:49], v[2:17]
	ds_read_b64_tr_b16 v[46:47],v197 offset:2048
	ds_read_b64_tr_b16 v[48:49],v197 offset:3072
	v_mfma_f32_32x32x16_f16 v[2:17], v[34:37], v[60:63], v[2:17]
	ds_read_b64_tr_b16 v[60:61],v197 offset:4096
	ds_read_b64_tr_b16 v[62:63],v197 offset:5120
	ds_read_b64_tr_b16 v[68:69],v197 offset:6144
	ds_read_b64_tr_b16 v[70:71],v197 offset:7168
	s_waitcnt lgkmcnt(0)
	v_mfma_f32_32x32x16_f16 v[2:17], v[38:41], v[64:67], v[2:17]
	v_mfma_f32_32x32x16_f16 v[18:33], v[52:55], v[42:45], v[18:33]
	v_mfma_f32_32x32x16_f16 v[18:33], v[56:59], v[46:49], v[18:33]
	v_mfma_f32_32x32x16_f16 v[18:33], v[34:37], v[60:63], v[18:33]
	v_mov_b32_e32 v34, v50
	s_nop 1
	v_permlane32_swap_b32_e32 v50, v34
	v_mfma_f32_32x32x16_f16 v[18:33], v[38:41], v[68:71], v[18:33]
	s_and_saveexec_b64 s[2:3], s[0:1]
	v_add_f32_e32 v34, v50, v34
	ds_write_b32 v204, v34 offset:49280
	s_or_b64 exec, exec, s[2:3]
	s_waitcnt lgkmcnt(0)
	ds_read_b128 v[34:37], v213 offset:49280
	ds_read_b128 v[38:41], v213 offset:49312
	s_lshl_b32 s20, s33, 12
	v_or_b32_e32 v50, s20, v201
	v_lshl_add_u32 v50, v191, 1, v50
	s_waitcnt lgkmcnt(1)
	v_rcp_f32_e32 v42, v34
	v_rcp_f32_e32 v43, v35
	v_rcp_f32_e32 v44, v36
	v_rcp_f32_e32 v45, v37
	v_fma_mixlo_f16 v2, v2, v42, 0
	ds_write_b16 v50, v2 offset:51200
	v_fma_mixlo_f16 v2, v18, v42, 0
	ds_write_b16 v50, v2 offset:51264
	v_fma_mixlo_f16 v2, v3, v43, 0
	ds_write_b16 v50, v2 offset:51328
	v_fma_mixlo_f16 v2, v19, v43, 0
	s_waitcnt lgkmcnt(3)
	v_rcp_f32_e32 v46, v38
	ds_write_b16 v50, v2 offset:51392
	v_fma_mixlo_f16 v2, v4, v44, 0
	ds_write_b16 v50, v2 offset:51456
	v_fma_mixlo_f16 v2, v20, v44, 0
	v_rcp_f32_e32 v47, v39
	ds_write_b16 v50, v2 offset:51520
	v_fma_mixlo_f16 v2, v5, v45, 0
	ds_read_b128 v[34:37], v213 offset:49344
	ds_write_b16 v50, v2 offset:51584
	v_fma_mixlo_f16 v2, v21, v45, 0
	v_rcp_f32_e32 v48, v40
	ds_write_b16 v50, v2 offset:51648
	v_fma_mixlo_f16 v2, v6, v46, 0
	ds_write_b16 v50, v2 offset:52224
	v_fma_mixlo_f16 v2, v22, v46, 0
	v_rcp_f32_e32 v49, v41
	ds_write_b16 v50, v2 offset:52288
	v_fma_mixlo_f16 v2, v7, v47, 0
	ds_write_b16 v50, v2 offset:52352
	v_fma_mixlo_f16 v2, v23, v47, 0
	ds_read_b128 v[38:41], v213 offset:49376
	s_waitcnt lgkmcnt(6)
	v_rcp_f32_e32 v34, v34
	ds_write_b16 v50, v2 offset:52416
	v_fma_mixlo_f16 v2, v8, v48, 0
	ds_write_b16 v50, v2 offset:52480
	v_fma_mixlo_f16 v2, v24, v48, 0
	v_rcp_f32_e32 v35, v35
	ds_write_b16 v50, v2 offset:52544
	v_fma_mixlo_f16 v2, v9, v49, 0
	ds_write_b16 v50, v2 offset:52608
	v_fma_mixlo_f16 v2, v25, v49, 0
	v_rcp_f32_e32 v36, v36
	ds_write_b16 v50, v2 offset:52672
	v_fma_mixlo_f16 v2, v10, v34, 0
	ds_write_b16 v50, v2 offset:53248
	v_fma_mixlo_f16 v2, v26, v34, 0
	v_rcp_f32_e32 v37, v37
	ds_write_b16 v50, v2 offset:53312
	v_fma_mixlo_f16 v2, v11, v35, 0
	ds_write_b16 v50, v2 offset:53376
	v_fma_mixlo_f16 v2, v27, v35, 0
	s_waitcnt lgkmcnt(8)
	v_rcp_f32_e32 v38, v38
	ds_write_b16 v50, v2 offset:53440
	v_fma_mixlo_f16 v2, v12, v36, 0
	ds_write_b16 v50, v2 offset:53504
	v_fma_mixlo_f16 v2, v28, v36, 0
	v_rcp_f32_e32 v39, v39
	ds_write_b16 v50, v2 offset:53568
	v_fma_mixlo_f16 v2, v13, v37, 0
	ds_write_b16 v50, v2 offset:53632
	v_fma_mixlo_f16 v2, v29, v37, 0
	v_rcp_f32_e32 v40, v40
	ds_write_b16 v50, v2 offset:53696
	v_fma_mixlo_f16 v2, v14, v38, 0
	ds_write_b16 v50, v2 offset:54272
	v_fma_mixlo_f16 v2, v30, v38, 0
	v_rcp_f32_e32 v41, v41
	ds_write_b16 v50, v2 offset:54336
	v_fma_mixlo_f16 v2, v15, v39, 0
	ds_write_b16 v50, v2 offset:54400
	v_fma_mixlo_f16 v2, v31, v39, 0
	ds_write_b16 v50, v2 offset:54464
	v_fma_mixlo_f16 v2, v16, v40, 0
	ds_write_b16 v50, v2 offset:54528
	v_fma_mixlo_f16 v2, v32, v40, 0
	ds_write_b16 v50, v2 offset:54592
	v_fma_mixlo_f16 v2, v17, v41, 0
	s_lshl_b64 s[2:3], s[18:19], 11
	ds_write_b16 v50, v2 offset:54656
	v_fma_mixlo_f16 v2, v33, v41, 0
	ds_write_b16 v50, v2 offset:54720
	s_or_b64 s[18:19], s[2:3], s[12:13]
	v_lshlrev_b32_e32 v2, 11, v0
	v_lshlrev_b32_e32 v213, 4, v1
	v_and_b32_e32 v2, 0x2000, v2
	v_mov_b32_e32 v195, 0
	s_add_u32 s18, s31, s18
	v_or_b32_e32 v14, s20, v213
	v_lshl_or_b32 v194, s30, 14, v2
	s_addc_u32 s19, 0, s19
	v_lshlrev_b32_e32 v2, 1, v193
	v_mov_b32_e32 v3, v195
	v_lshlrev_b32_e32 v214, 7, v190
	s_waitcnt lgkmcnt(0)
	v_lshl_add_u64 v[10:11], s[18:19], 0, v[194:195]
	v_lshl_add_u64 v[188:189], s[6:7], 0, v[2:3]
	v_or_b32_e32 v2, v14, v214
	ds_read_b128 v[2:5], v2 offset:51200
	v_or_b32_e32 v6, v10, v190
	v_mov_b32_e32 v7, v11
	v_or_b32_e32 v196, 8, v190
	v_lshlrev_b64 v[6:7], 6, v[6:7]
	v_lshlrev_b32_e32 v215, 7, v196
	v_lshl_add_u64 v[12:13], v[188:189], 0, v[6:7]
	v_or_b32_e32 v6, v14, v215
	ds_read_b128 v[6:9], v6 offset:51200
	s_waitcnt lgkmcnt(1)
	global_store_dwordx4 v[12:13], v[2:5], off sc1
	v_or_b32_e32 v198, 16, v190
	v_lshlrev_b32_e32 v216, 7, v198
	v_or_b32_e32 v2, v10, v196
	v_mov_b32_e32 v3, v11
	v_lshlrev_b64 v[2:3], 6, v[2:3]
	v_lshl_add_u64 v[2:3], v[188:189], 0, v[2:3]
	s_waitcnt lgkmcnt(0)
	global_store_dwordx4 v[2:3], v[6:9], off sc1
	v_or_b32_e32 v2, v14, v216
	v_or_b32_e32 v200, 24, v190
	v_or_b32_e32 v6, v10, v198
	v_mov_b32_e32 v7, v11
	ds_read_b128 v[2:5], v2 offset:51200
	v_lshlrev_b64 v[6:7], 6, v[6:7]
	v_lshlrev_b32_e32 v217, 7, v200
	v_lshl_add_u64 v[12:13], v[188:189], 0, v[6:7]
	v_or_b32_e32 v6, v14, v217
	ds_read_b128 v[6:9], v6 offset:51200
	v_or_b32_e32 v10, v10, v200
	s_waitcnt lgkmcnt(1)
	global_store_dwordx4 v[12:13], v[2:5], off sc1
	v_readfirstlane_b32 s20, v0
	s_lshr_b32 s19, s20, 6
	v_lshlrev_b64 v[2:3], 6, v[10:11]
	v_lshl_add_u64 v[2:3], v[188:189], 0, v[2:3]
	s_waitcnt lgkmcnt(0)
	global_store_dwordx4 v[2:3], v[6:9], off sc1
	v_lshl_or_b32 v2, s19, 3, v190
	s_xor_b32 s6, s12, 0x700
	v_mov_b32_e32 v3, v195
	v_lshrrev_b32_e32 v88, 1, v2
	s_or_b32 s7, s8, s6
	s_lshl_b32 s18, s19, 5
	v_lshlrev_b64 v[84:85], 7, v[2:3]
	v_xor_b32_e32 v2, v88, v0
	s_add_u32 s8, s7, s18
	v_lshlrev_b32_e32 v2, 4, v2
	s_addc_u32 s9, s9, 0
	v_lshl_add_u64 v[4:5], s[14:15], 0, v[84:85]
	v_and_b32_e32 v2, 0x70, v2
	s_lshl_b64 s[8:9], s[8:9], 7
	v_lshl_add_u64 v[184:185], v[4:5], 0, v[2:3]
	v_lshlrev_b32_e32 v4, 1, v190
	s_waitcnt lgkmcnt(0)
	s_barrier
	s_cmp_lg_u32 s91, 0
	s_cbranch_scc1 .Lattn_done
	s_movk_i32 s91, 0x700
	s_mov_b64 s[0:1], s[88:89]
	s_mov_b32 s2, s87
	s_branch .Lattn_unit2
